# grid barriers FFN-up to FFN-down, rec-in to gates and gates to rec-out release per XCD when the workgroup numbering is XCD-consistent (row panels stay on one XCD, no overlaid buffers between those pha
# speedup vs baseline: 1.0006x; 1.0002x over previous
; __device__ __forceinline__ unsigned xb_ld(unsigned* p)              { return __hip_atomic_load(p, __ATOMIC_RELAXED, __HIP_MEMORY_SCOPE_AGENT); }
; __device__ __forceinline__ unsigned xb_add(unsigned* p, unsigned v) { return __hip_atomic_fetch_add(p, v, __ATOMIC_RELAXED, __HIP_MEMORY_SCOPE_AGENT); }
; #define XB_SPIN(cond, bar) do { unsigned _sp = 0; while (cond) { __builtin_amdgcn_s_sleep(1); \
;     if ((++_sp & 255u) == 0u) { if (xb_ld(&(bar)[XB_TMO])) break; if (_sp > XB_SPIN_CAP) { atomicAdd(&(bar)[XB_TMO], 1u); break; } } } } while (0)
; __device__ __forceinline__ void xcd_barrier(const XcdBarrier& b) {
;     ...
;         const unsigned old = xb_add(&bar[XB_XSUB(b.x)], 1u);
;         const unsigned gen = old / nloc;
;         if (old + 1u == (gen + 1u) * nloc) {
;             __builtin_amdgcn_fence(__ATOMIC_RELEASE, "agent");
;             asm volatile("s_waitcnt vmcnt(0)" ::: "memory");
;             const unsigned og = xb_add(&bar[XB_TOP], 1u);
;             const unsigned tg = og / nx;
;             if (og + 1u == (tg + 1u) * nx) xb_add(&bar[XB_TOPGEN], 1u);
;             else XB_SPIN(xb_ld(&bar[XB_TOPGEN]) == tg, bar);
.LBB0_1293:
	s_andn2_saveexec_b64 s[8:9], s[8:9]
	s_cbranch_execz .LBB0_1313
	s_mov_b64 s[8:9], exec
	buffer_wbl2 sc1
	s_waitcnt lgkmcnt(0)
	s_waitcnt vmcnt(0)
	v_readlane_b32 s12, v254, 14
	s_cmp_lg_u32 s12, 0
	s_cbranch_scc1 .Lxcdlocal_0
	v_mbcnt_lo_u32_b32 v1, s8, 0
	v_mbcnt_hi_u32_b32 v1, s9, v1
	v_cmp_eq_u32_e32 vcc, 0, v1
	s_and_saveexec_b64 s[10:11], vcc
	s_cbranch_execz .LBB0_1296
	s_bcnt1_i32_b64 s8, s[8:9]
	v_mov_b32_e32 v3, s8
	v_readlane_b32 s8, v254, 4
	v_mov_b32_e32 v2, 0x7000
	v_readlane_b32 s9, v254, 5
	s_nop 4
	global_atomic_add v2, v2, v3, s[8:9] offset:1024 sc0

; __device__ __forceinline__ unsigned xb_add(unsigned* p, unsigned v) { return __hip_atomic_fetch_add(p, v, __ATOMIC_RELAXED, __HIP_MEMORY_SCOPE_AGENT); }
; __device__ __forceinline__ void xcd_barrier(const XcdBarrier& b) {
;     ...
;             __builtin_amdgcn_fence(__ATOMIC_ACQUIRE, "agent");
;             xb_add(&bar[XB_XGEN(b.x)], 1u);
;             asm volatile("s_waitcnt vmcnt(0)" ::: "memory");
.Lxcdlocal_0:
	s_mov_b64 s[8:9], exec
	v_mbcnt_lo_u32_b32 v0, s8, 0
	v_mbcnt_hi_u32_b32 v0, s9, v0
	v_cmp_eq_u32_e32 vcc, 0, v0
	s_waitcnt vmcnt(0)
	buffer_inv sc1
	s_and_saveexec_b64 s[10:11], vcc
	s_cbranch_execz .LBB0_1312
	s_bcnt1_i32_b64 s8, s[8:9]
	v_mov_b32_e32 v0, 0x2000
	v_mov_b32_e32 v1, s8
	global_atomic_add v0, v1, s[6:7] offset:1024

; __device__ __forceinline__ unsigned xb_add(unsigned* p, unsigned v) { return __hip_atomic_fetch_add(p, v, __ATOMIC_RELAXED, __HIP_MEMORY_SCOPE_AGENT); }
; __device__ __forceinline__ void xcd_barrier(const XcdBarrier& b) {
;     ...
;             __builtin_amdgcn_fence(__ATOMIC_ACQUIRE, "agent");
;             xb_add(&bar[XB_XGEN(b.x)], 1u);
;             asm volatile("s_waitcnt vmcnt(0)" ::: "memory");
.Lxcdlocal_1:
	s_mov_b64 s[8:9], exec
	v_mbcnt_lo_u32_b32 v0, s8, 0
	v_mbcnt_hi_u32_b32 v0, s9, v0
	v_cmp_eq_u32_e32 vcc, 0, v0
	s_waitcnt vmcnt(0)
	buffer_inv sc1
	s_and_saveexec_b64 s[10:11], vcc
	s_cbranch_execz .LBB0_1574
	s_bcnt1_i32_b64 s8, s[8:9]
	v_mov_b32_e32 v0, 0x2000
	v_mov_b32_e32 v1, s8
	global_atomic_add v0, v1, s[2:3] offset:1024

; __device__ __forceinline__ unsigned xb_ld(unsigned* p)              { return __hip_atomic_load(p, __ATOMIC_RELAXED, __HIP_MEMORY_SCOPE_AGENT); }
; __device__ __forceinline__ unsigned xb_add(unsigned* p, unsigned v) { return __hip_atomic_fetch_add(p, v, __ATOMIC_RELAXED, __HIP_MEMORY_SCOPE_AGENT); }
; #define XB_SPIN(cond, bar) do { unsigned _sp = 0; while (cond) { __builtin_amdgcn_s_sleep(1); \
;     if ((++_sp & 255u) == 0u) { if (xb_ld(&(bar)[XB_TMO])) break; if (_sp > XB_SPIN_CAP) { atomicAdd(&(bar)[XB_TMO], 1u); break; } } } } while (0)
; __device__ __forceinline__ void xcd_barrier(const XcdBarrier& b) {
;     ...
;         const unsigned old = xb_add(&bar[XB_XSUB(b.x)], 1u);
;         const unsigned gen = old / nloc;
;         if (old + 1u == (gen + 1u) * nloc) {
;             __builtin_amdgcn_fence(__ATOMIC_RELEASE, "agent");
;             asm volatile("s_waitcnt vmcnt(0)" ::: "memory");
;             const unsigned og = xb_add(&bar[XB_TOP], 1u);
;             const unsigned tg = og / nx;
;             if (og + 1u == (tg + 1u) * nx) xb_add(&bar[XB_TOPGEN], 1u);
;             else XB_SPIN(xb_ld(&bar[XB_TOPGEN]) == tg, bar);
.LBB0_1712:
	s_andn2_saveexec_b64 s[6:7], s[6:7]
	s_cbranch_execz .LBB0_1732
	s_mov_b64 s[6:7], exec
	buffer_wbl2 sc1
	s_waitcnt lgkmcnt(0)
	s_waitcnt vmcnt(0)
	v_readlane_b32 s10, v254, 14
	s_cmp_lg_u32 s10, 0
	s_cbranch_scc1 .Lxcdlocal_2
	v_mbcnt_lo_u32_b32 v1, s6, 0
	v_mbcnt_hi_u32_b32 v1, s7, v1
	v_cmp_eq_u32_e32 vcc, 0, v1
	s_and_saveexec_b64 s[8:9], vcc
	s_cbranch_execz .LBB0_1715
	s_bcnt1_i32_b64 s6, s[6:7]
	v_mov_b32_e32 v3, s6
	v_readlane_b32 s6, v254, 4
	v_mov_b32_e32 v2, 0x7000
	v_readlane_b32 s7, v254, 5
	s_nop 4
	global_atomic_add v2, v2, v3, s[6:7] offset:1024 sc0

; __device__ __forceinline__ unsigned xb_add(unsigned* p, unsigned v) { return __hip_atomic_fetch_add(p, v, __ATOMIC_RELAXED, __HIP_MEMORY_SCOPE_AGENT); }
; __device__ __forceinline__ void xcd_barrier(const XcdBarrier& b) {
;     ...
;             __builtin_amdgcn_fence(__ATOMIC_ACQUIRE, "agent");
;             xb_add(&bar[XB_XGEN(b.x)], 1u);
;             asm volatile("s_waitcnt vmcnt(0)" ::: "memory");
.Lxcdlocal_2:
	s_mov_b64 s[6:7], exec
	v_mbcnt_lo_u32_b32 v0, s6, 0
	v_mbcnt_hi_u32_b32 v0, s7, v0
	v_cmp_eq_u32_e32 vcc, 0, v0
	s_waitcnt vmcnt(0)
	buffer_inv sc1
	s_and_saveexec_b64 s[8:9], vcc
	s_cbranch_execz .LBB0_1731
	s_bcnt1_i32_b64 s6, s[6:7]
	v_mov_b32_e32 v0, 0x2000
	v_mov_b32_e32 v1, s6
	global_atomic_add v0, v1, s[2:3] offset:1024
